# P10: first two DMA waits of each unit's peeled first K iteration dropped (prefetch already waited for at the epilogue top; they only waited for store acks)
# baseline (speedup 1.0000x reference)
; #define PG8_STAGE2(bufoff, gbase, v0, v1) do { \
;         __builtin_amdgcn_global_load_lds((const unsigned*)((const char*)(gbase) + (v0)), (LAS unsigned*)(lds + (bufoff) + ldsw), 16, 0, 0); \
;         __builtin_amdgcn_global_load_lds((const unsigned*)((const char*)(gbase) + (v1)), (LAS unsigned*)(lds + (bufoff) + ldsw + 8192), 16, 0, 0); } while (0)
; #define PG8_STAGE(bufoff, gbase, voff) PG8_STAGE2(bufoff, gbase, (voff)[0], (voff)[1])
; #define PG8_WAIT_V(n) asm volatile("s_waitcnt vmcnt(" #n ")" ::: "memory")
; #define PG8_BAR __builtin_amdgcn_s_barrier()
; template <class Epi, class Sched, bool ALIGN_EPI, bool SP2, bool GATHER>
; DI void gemm_phase(LAS unsigned char* lds, const Gemm g, const Sched& S, const Epi& E) {
;     ...
;     const unsigned ldsw = (unsigned)wid * 1024u;
;     const int aoff = lds_byte(wr * 64 + fr, fq * 8), boff = lds_byte(wc * 32 + fr, fq * 8);
;     ...
;     PG8_STAGE(PG8_SB(0, 0), cB, voffB); PG8_STAGE(PG8_SB(0, 1), cB + hstep, voffB); PG8_STAGE2(PG8_SA(0, 0), cA, gC[0][0], gC[0][1]); PG8_STAGE2(PG8_SA(0, 1), cA + hstepA, gC[1][0], gC[1][1]);
;     if (wr == 1) PG8_BAR;
;     PG8_WAIT_V(2); PG8_BAR;
;     PG8_STAGE(PG8_SB(1, 0), cB + kstep, voffB); PG8_STAGE2(PG8_SA(1, 0), cA + kstep, gC[0][0], gC[0][1]); PG8_STAGE(PG8_SB(1, 1), cB + hstep + kstep, voffB);
;     PG8_WAIT_V(6); PG8_BAR;
.LBB0_990:
	s_waitcnt lgkmcnt(0)
	s_add_u32 s4, s12, 0x240000
	s_addc_u32 s5, s13, 0
	s_add_u32 s6, s10, 0x280000
	s_addc_u32 s7, s11, 0
	s_add_u32 s8, s8, 0x2000000
	s_addc_u32 s9, s9, 0
	s_lshl_b32 s10, s16, 5
	s_and_b32 s16, s10, 0x60
	s_mov_b64 s[10:11], 0x80
	v_lshl_add_u64 v[8:9], v[8:9], 0, s[10:11]
	s_add_i32 m0, s27, 0x18000
	s_lshl_b32 s17, s15, 13
	s_lshl_b32 s18, s16, 7
	s_waitcnt vmcnt(2)
	s_barrier
	global_load_lds_dwordx4 v[8:9], off
	v_lshl_add_u64 v[6:7], v[6:7], 0, s[10:11]
	s_add_i32 m0, s27, 0x1a000
	s_add_i32 s46, s27, 0x8000
	s_add_i32 s47, s27, 0xa000
	global_load_lds_dwordx4 v[6:7], off
	v_lshl_add_u64 v[2:3], v[2:3], 0, s[10:11]
	s_mov_b32 m0, s46
	s_add_u32 s12, s30, 0x20080
	global_load_lds_dwordx4 v[2:3], off
	v_lshl_add_u64 v[2:3], v[4:5], 0, s[10:11]
	s_mov_b32 m0, s47
	s_addc_u32 s13, s31, 0
	global_load_lds_dwordx4 v[2:3], off
	v_lshl_add_u64 v[2:3], s[12:13], 0, v[132:133]
	s_add_i32 m0, s27, 0x1c000
	v_lshlrev_b32_e32 v4, 2, v0
	global_load_lds_dwordx4 v[2:3], off
	v_lshl_add_u64 v[2:3], s[12:13], 0, v[136:137]
	s_add_i32 m0, s27, 0x1e000
	v_lshlrev_b32_e32 v5, 6, v0
	global_load_lds_dwordx4 v[2:3], off
	v_and_b32_e32 v2, 15, v0
	v_lshlrev_b32_e32 v3, 1, v13
	s_movk_i32 s12, 0x3c0
	v_lshl_or_b32 v1, s15, 6, v2
	v_lshl_or_b32 v2, v2, 6, v3
	v_and_b32_e32 v4, 32, v4
	v_and_or_b32 v3, v5, s12, v3
	v_bitop3_b32 v152, s18, v3, v4 bitop3:0xf6
	v_lshlrev_b32_e32 v3, 7, v0
	v_bitop3_b32 v2, v2, s17, v4 bitop3:0xde
	v_and_b32_e32 v3, 0xc000, v3
	v_lshlrev_b32_e32 v4, 10, v12
	v_or3_b32 v3, v10, v3, v4
	v_add_u32_e32 v140, v3, v11
	v_lshlrev_b32_e32 v3, 3, v14
	s_waitcnt vmcnt(0)
	s_cmpk_lt_u32 s14, 0x100
	v_and_b32_e32 v3, 0x1c000, v3
	s_cselect_b64 s[12:13], -1, 0
	v_or3_b32 v3, v10, v3, v4
	s_add_i32 s48, 0, 0x10000
	s_add_i32 s49, 0, 0x14000
	v_or_b32_e32 v153, s16, v13
	v_mov_b32_e32 v141, v139
	v_add_u32_e32 v142, v3, v11
	v_mov_b32_e32 v143, v139
	v_add_u32_e32 v154, s48, v152
	v_add_u32_e32 v155, s49, v152
	v_add_u32_e32 v156, 0, v2
	s_barrier
	s_branch .LBB0_993

; #define PG8_STAGE2(bufoff, gbase, v0, v1) do { \
;         __builtin_amdgcn_global_load_lds((const unsigned*)((const char*)(gbase) + (v0)), (LAS unsigned*)(lds + (bufoff) + ldsw), 16, 0, 0); \
;         __builtin_amdgcn_global_load_lds((const unsigned*)((const char*)(gbase) + (v1)), (LAS unsigned*)(lds + (bufoff) + ldsw + 8192), 16, 0, 0); } while (0)
; #define PG8_STAGE(bufoff, gbase, voff) PG8_STAGE2(bufoff, gbase, (voff)[0], (voff)[1])
; #define PG8_LDA(dst, b, h) do { _Pragma("unroll") for (int m = 0; m < 4; ++m) _Pragma("unroll") for (int k = 0; k < 2; ++k) dst[m][k] = *(const LAS bf16x8*)(lds + PG8_SA(b, h) + aoff + m * 2048 + k * 1024); } while (0)
; #define PG8_BAR __builtin_amdgcn_s_barrier()
; template <class Epi, class Sched, bool ALIGN_EPI, bool SP2, bool GATHER>
; DI void gemm_phase(LAS unsigned char* lds, const Gemm g, const Sched& S, const Epi& E) {
;     ...
;         const bool has_next = S.next(ui + 1, nxt);
;         const char* nA = (has_next && !GATHER) ? (const char*)g.A + (size_t)nxt.pm * tstep : cA; const char* nB = has_next ? (const char*)g.Bt + (size_t)nxt.pn * tstep : cB;
;         if constexpr (GATHER) { if (has_next) { PG8_GATHER(nxt, gN); } else {
; #pragma unroll
;             for (int h = 0; h < 2; ++h) { gN[h][0] = gC[h][0]; gN[h][1] = gC[h][1]; } } }
;         for (int t = 0; t < nt; t += 2) {
;             if constexpr (Epi::MID_T >= 0) { if (t == Epi::MID_T) { E.mid(acc, cur, wr, wc, fr, fq); PG8_SCHED; } }
;             const bool last = (t == nt - 2);
;             const char* a1 = cA + (size_t)(t + 1) * kstep;
;             const char* a2 = last ? nA : cA + (size_t)(t + 2) * kstep; const char* b2 = last ? nB : cB + (size_t)(t + 2) * kstep;
;             const char* a3 = a2 + kstep; const char* b3 = b2 + kstep;
;             unsigned x00 = gC[0][0], x01 = gC[0][1], x10 = gC[1][0], x11 = gC[1][1];
;             if constexpr (GATHER) { if (last) { x00 = gN[0][0]; x01 = gN[0][1]; x10 = gN[1][0]; x11 = gN[1][1]; } }
;             PG8_LDB(B0, 0, 0); PG8_LDB(B1, 0, 1); PG8_SCHED; PG8_LDA(At, 0, 0); PG8_STAGE2(PG8_SA(1, 1), a1 + hstepA, gC[1][0], gC[1][1]);
;             PG8_WAIT_V(8); PG8_WAIT_L(0); PG8_BAR; PG8_MMA(0, 0, At, B0); PG8_MMA(0, 1, At, B1); PG8_BAR; PG8_SCHED;
;             PG8_LDA(At, 0, 1); PG8_STAGE(PG8_SB(0, 0), b2, voffB); PG8_STAGE(PG8_SB(0, 1), b2 + hstep, voffB); PG8_STAGE2(PG8_SA(0, 0), a2, x00, x01);
.LBB0_995:
	s_ashr_i32 s15, s14, 31
	s_lshl_b64 s[20:21], s[14:15], 18
	s_add_u32 s20, s37, s20
	s_addc_u32 s21, s38, s21
	s_and_b64 s[22:23], s[18:19], exec
	s_cselect_b32 s15, s21, s29
	s_cselect_b32 s25, s20, s28
	s_ashr_i32 s17, s16, 31
	s_lshl_b64 s[22:23], s[16:17], 18
	s_add_u32 s22, s39, s22
	s_addc_u32 s23, s40, s23
	s_and_b64 s[34:35], s[18:19], exec
	s_cselect_b32 s17, s23, s31
	s_cselect_b32 s50, s22, s30
	s_add_u32 s28, s28, 0x20080
	s_addc_u32 s29, s29, 0
	s_add_u32 s51, s30, 0x100
	s_addc_u32 s52, s31, 0
	s_mov_b32 s53, -2
	ds_read_b128 v[144:147], v154
	ds_read_b128 v[148:151], v154 offset:1024
	ds_read_b128 v[158:161], v154 offset:2048
	ds_read_b128 v[162:165], v154 offset:3072
	ds_read_b128 v[166:169], v155
	ds_read_b128 v[170:173], v155 offset:1024
	ds_read_b128 v[174:177], v155 offset:2048
	ds_read_b128 v[178:181], v155 offset:3072
	s_add_u32 s30, s28, 0xfffe0080
	s_addc_u32 s31, s29, -1
	s_cmp_eq_u32 s53, 4
	s_cselect_b32 s35, s15, s31
	s_cselect_b32 s34, s25, s30
	s_cselect_b32 s31, s17, s52
	s_cselect_b32 s30, s50, s51
	v_lshl_add_u64 v[214:215], s[28:29], 0, v[140:141]
	s_add_i32 m0, s27, 0xc000
	ds_read_b128 v[182:185], v156
	ds_read_b128 v[186:189], v156 offset:1024
	ds_read_b128 v[190:193], v156 offset:2048
	ds_read_b128 v[194:197], v156 offset:3072
	ds_read_b128 v[198:201], v156 offset:4096
	ds_read_b128 v[202:205], v156 offset:5120
	ds_read_b128 v[206:209], v156 offset:6144
	ds_read_b128 v[210:213], v156 offset:7168
	global_load_lds_dwordx4 v[214:215], off
	v_lshl_add_u64 v[214:215], s[28:29], 0, v[142:143]
	s_add_i32 m0, s27, 0xe000
	s_nop 0
	global_load_lds_dwordx4 v[214:215], off
	s_nop 0
	s_waitcnt lgkmcnt(0)
	s_barrier
	s_setprio 1
	s_waitcnt lgkmcnt(0)
	v_mfma_f32_16x16x32_bf16 v[126:129], v[144:147], v[182:185], 0
	v_mfma_f32_16x16x32_bf16 v[122:125], v[158:161], v[182:185], 0
	v_mfma_f32_16x16x32_bf16 v[110:113], v[144:147], v[190:193], 0
	v_mfma_f32_16x16x32_bf16 v[106:109], v[158:161], v[190:193], 0
	v_mfma_f32_16x16x32_bf16 v[94:97], v[144:147], v[198:201], 0
	v_mfma_f32_16x16x32_bf16 v[90:93], v[158:161], v[198:201], 0
	v_mfma_f32_16x16x32_bf16 v[78:81], v[144:147], v[206:209], 0
	v_mfma_f32_16x16x32_bf16 v[74:77], v[158:161], v[206:209], 0
	v_mfma_f32_16x16x32_bf16 v[126:129], v[148:151], v[186:189], v[126:129]
	v_mfma_f32_16x16x32_bf16 v[122:125], v[162:165], v[186:189], v[122:125]
	v_mfma_f32_16x16x32_bf16 v[110:113], v[148:151], v[194:197], v[110:113]
	v_mfma_f32_16x16x32_bf16 v[106:109], v[162:165], v[194:197], v[106:109]
	v_mfma_f32_16x16x32_bf16 v[94:97], v[148:151], v[202:205], v[94:97]
	v_mfma_f32_16x16x32_bf16 v[90:93], v[162:165], v[202:205], v[90:93]
	v_mfma_f32_16x16x32_bf16 v[78:81], v[148:151], v[210:213], v[78:81]
	v_mfma_f32_16x16x32_bf16 v[74:77], v[162:165], v[210:213], v[74:77]
	s_setprio 0
	s_setprio 1
	v_mfma_f32_16x16x32_bf16 v[118:121], v[166:169], v[182:185], 0
	v_mfma_f32_16x16x32_bf16 v[114:117], v[174:177], v[182:185], 0
	v_mfma_f32_16x16x32_bf16 v[102:105], v[166:169], v[190:193], 0
	v_mfma_f32_16x16x32_bf16 v[98:101], v[174:177], v[190:193], 0
	v_mfma_f32_16x16x32_bf16 v[86:89], v[166:169], v[198:201], 0
	v_mfma_f32_16x16x32_bf16 v[82:85], v[174:177], v[198:201], 0
	v_mfma_f32_16x16x32_bf16 v[70:73], v[166:169], v[206:209], 0
	v_mfma_f32_16x16x32_bf16 v[66:69], v[174:177], v[206:209], 0
	v_mfma_f32_16x16x32_bf16 v[118:121], v[170:173], v[186:189], v[118:121]
	v_mfma_f32_16x16x32_bf16 v[114:117], v[178:181], v[186:189], v[114:117]
	v_mfma_f32_16x16x32_bf16 v[102:105], v[170:173], v[194:197], v[102:105]
	v_mfma_f32_16x16x32_bf16 v[98:101], v[178:181], v[194:197], v[98:101]
	v_mfma_f32_16x16x32_bf16 v[86:89], v[170:173], v[202:205], v[86:89]
	v_mfma_f32_16x16x32_bf16 v[82:85], v[178:181], v[202:205], v[82:85]
	v_mfma_f32_16x16x32_bf16 v[70:73], v[170:173], v[210:213], v[70:73]
	v_mfma_f32_16x16x32_bf16 v[66:69], v[178:181], v[210:213], v[66:69]
	s_setprio 0
	s_barrier
	s_add_i32 s54, s48, s41
	v_lshl_add_u64 v[214:215], s[30:31], 0, v[132:133]
	s_mov_b32 m0, s54
	ds_read_b128 v[182:185], v156 offset:16384
	ds_read_b128 v[186:189], v156 offset:17408
	ds_read_b128 v[190:193], v156 offset:18432
	ds_read_b128 v[194:197], v156 offset:19456
	ds_read_b128 v[198:201], v156 offset:20480
	ds_read_b128 v[202:205], v156 offset:21504
	ds_read_b128 v[206:209], v156 offset:22528
	ds_read_b128 v[210:213], v156 offset:23552
	global_load_lds_dwordx4 v[214:215], off
	s_add_i32 m0, s54, 0x2000
	s_add_u32 s54, s30, 0x20000
	v_lshl_add_u64 v[216:217], s[30:31], 0, v[136:137]
	s_addc_u32 s55, s31, 0
	s_add_i32 s56, s49, s41
	global_load_lds_dwordx4 v[216:217], off
	v_lshl_add_u64 v[218:219], s[54:55], 0, v[132:133]
	s_mov_b32 m0, s56
	v_lshl_add_u64 v[220:221], s[34:35], 0, v[134:135]
	global_load_lds_dwordx4 v[218:219], off
	v_lshl_add_u64 v[218:219], s[54:55], 0, v[136:137]
	s_add_i32 m0, s56, 0x2000
	s_nop 0
	global_load_lds_dwordx4 v[218:219], off
	v_lshl_add_u64 v[218:219], s[34:35], 0, v[130:131]
	s_mov_b32 m0, s27
	s_nop 0
	global_load_lds_dwordx4 v[218:219], off
	s_mov_b32 m0, s42
	s_nop 0
	global_load_lds_dwordx4 v[220:221], off
	s_nop 0
	s_waitcnt lgkmcnt(0)
	s_barrier
; #define PG8_STAGE2(bufoff, gbase, v0, v1) do { \
;         __builtin_amdgcn_global_load_lds((const unsigned*)((const char*)(gbase) + (v0)), (LAS unsigned*)(lds + (bufoff) + ldsw), 16, 0, 0); \
;         __builtin_amdgcn_global_load_lds((const unsigned*)((const char*)(gbase) + (v1)), (LAS unsigned*)(lds + (bufoff) + ldsw + 8192), 16, 0, 0); } while (0)
; #define PG8_LDA(dst, b, h) do { _Pragma("unroll") for (int m = 0; m < 4; ++m) _Pragma("unroll") for (int k = 0; k < 2; ++k) dst[m][k] = *(const LAS bf16x8*)(lds + PG8_SA(b, h) + aoff + m * 2048 + k * 1024); } while (0)
; #define PG8_LDB(dst, b, h) do { _Pragma("unroll") for (int n = 0; n < 2; ++n) _Pragma("unroll") for (int k = 0; k < 2; ++k) dst[n][k] = *(const LAS bf16x8*)(lds + PG8_SB(b, h) + boff + n * 2048 + k * 1024); } while (0)
; #define PG8_MMA(ai, bj, At, Bt) do { __builtin_amdgcn_s_setprio(1); _Pragma("unroll") for (int m = 0; m < 4; ++m) _Pragma("unroll") for (int n = 0; n < 2; ++n) _Pragma("unroll") for (int k = 0; k < 2; ++k) \
;         acc[ai][bj][m][n] = __builtin_amdgcn_mfma_f32_16x16x32_bf16(Bt[n][k], At[m][k], acc[ai][bj][m][n], 0, 0, 0); __builtin_amdgcn_s_setprio(0); } while (0)
; #define PG8_WAIT_V(n) asm volatile("s_waitcnt vmcnt(" #n ")" ::: "memory")
; #define PG8_WAIT_L(n) asm volatile("s_waitcnt lgkmcnt(" #n ")" ::: "memory")
; #define PG8_BAR __builtin_amdgcn_s_barrier()
; #define PG8_SCHED __builtin_amdgcn_sched_barrier(0)
; template <class Epi, class Sched, bool ALIGN_EPI, bool SP2, bool GATHER>
; DI void gemm_phase(LAS unsigned char* lds, const Gemm g, const Sched& S, const Epi& E) {
;     ...
;             PG8_WAIT_V(8); PG8_WAIT_L(0); PG8_BAR; PG8_MMA(1, 0, At, B0); PG8_MMA(1, 1, At, B1); PG8_BAR; PG8_SCHED;
;             PG8_LDB(B0, 1, 0); PG8_LDB(B1, 1, 1); PG8_SCHED; PG8_LDA(At, 1, 0); PG8_STAGE2(PG8_SA(0, 1), a2 + hstepA, x10, x11);
;             PG8_WAIT_V(8); PG8_WAIT_L(0); PG8_BAR; PG8_MMA(0, 0, At, B0); PG8_MMA(0, 1, At, B1); PG8_BAR; PG8_SCHED;
	s_setprio 1
	s_waitcnt lgkmcnt(0)
	v_mfma_f32_16x16x32_bf16 v[62:65], v[144:147], v[182:185], 0
	v_mfma_f32_16x16x32_bf16 v[58:61], v[158:161], v[182:185], 0
	v_mfma_f32_16x16x32_bf16 v[46:49], v[144:147], v[190:193], 0
	v_mfma_f32_16x16x32_bf16 v[42:45], v[158:161], v[190:193], 0
	v_mfma_f32_16x16x32_bf16 v[14:17], v[144:147], v[198:201], 0
	v_mfma_f32_16x16x32_bf16 v[10:13], v[158:161], v[198:201], 0
	v_mfma_f32_16x16x32_bf16 v[6:9], v[144:147], v[206:209], 0
	v_mfma_f32_16x16x32_bf16 v[2:5], v[158:161], v[206:209], 0
	v_mfma_f32_16x16x32_bf16 v[62:65], v[148:151], v[186:189], v[62:65]
	v_mfma_f32_16x16x32_bf16 v[58:61], v[162:165], v[186:189], v[58:61]
	v_mfma_f32_16x16x32_bf16 v[46:49], v[148:151], v[194:197], v[46:49]
	v_mfma_f32_16x16x32_bf16 v[42:45], v[162:165], v[194:197], v[42:45]
	v_mfma_f32_16x16x32_bf16 v[14:17], v[148:151], v[202:205], v[14:17]
	v_mfma_f32_16x16x32_bf16 v[10:13], v[162:165], v[202:205], v[10:13]
	v_mfma_f32_16x16x32_bf16 v[6:9], v[148:151], v[210:213], v[6:9]
	v_mfma_f32_16x16x32_bf16 v[2:5], v[162:165], v[210:213], v[2:5]
	s_setprio 0
	s_setprio 1
	v_mfma_f32_16x16x32_bf16 v[54:57], v[166:169], v[182:185], 0
	v_mfma_f32_16x16x32_bf16 v[50:53], v[174:177], v[182:185], 0
	v_mfma_f32_16x16x32_bf16 v[30:33], v[166:169], v[190:193], 0
	v_mfma_f32_16x16x32_bf16 v[26:29], v[174:177], v[190:193], 0
	v_mfma_f32_16x16x32_bf16 v[34:37], v[166:169], v[198:201], 0
	v_mfma_f32_16x16x32_bf16 v[38:41], v[174:177], v[198:201], 0
	v_mfma_f32_16x16x32_bf16 v[18:21], v[166:169], v[206:209], 0
	v_mfma_f32_16x16x32_bf16 v[22:25], v[174:177], v[206:209], 0
	v_mfma_f32_16x16x32_bf16 v[54:57], v[170:173], v[186:189], v[54:57]
	v_mfma_f32_16x16x32_bf16 v[50:53], v[178:181], v[186:189], v[50:53]
	v_mfma_f32_16x16x32_bf16 v[30:33], v[170:173], v[194:197], v[30:33]
	v_mfma_f32_16x16x32_bf16 v[26:29], v[178:181], v[194:197], v[26:29]
	v_mfma_f32_16x16x32_bf16 v[34:37], v[170:173], v[202:205], v[34:37]
	v_mfma_f32_16x16x32_bf16 v[38:41], v[178:181], v[202:205], v[38:41]
	v_mfma_f32_16x16x32_bf16 v[18:21], v[170:173], v[210:213], v[18:21]
	v_mfma_f32_16x16x32_bf16 v[22:25], v[178:181], v[210:213], v[22:25]
	s_setprio 0
	s_barrier
	s_add_i32 s54, 0, 0x18000
	v_add_u32_e32 v138, s54, v152
	s_add_i32 s55, 0, 0x1c000
	ds_read_b128 v[144:147], v138
	ds_read_b128 v[148:151], v138 offset:1024
	ds_read_b128 v[158:161], v138 offset:2048
	ds_read_b128 v[162:165], v138 offset:3072
	v_add_u32_e32 v138, s55, v152
	ds_read_b128 v[166:169], v138
	ds_read_b128 v[170:173], v138 offset:1024
	ds_read_b128 v[174:177], v138 offset:2048
	ds_read_b128 v[178:181], v138 offset:3072
	s_add_u32 s34, s34, 0x20000
	s_addc_u32 s35, s35, 0
	s_mov_b32 m0, s43
	v_lshl_add_u64 v[222:223], s[34:35], 0, v[130:131]
	ds_read_b128 v[182:185], v156 offset:32768
	ds_read_b128 v[186:189], v156 offset:33792
	ds_read_b128 v[190:193], v156 offset:34816
	ds_read_b128 v[194:197], v156 offset:35840
	ds_read_b128 v[198:201], v156 offset:36864
	ds_read_b128 v[202:205], v156 offset:37888
	ds_read_b128 v[206:209], v156 offset:38912
	ds_read_b128 v[210:213], v156 offset:39936
	global_load_lds_dwordx4 v[222:223], off
	v_lshl_add_u64 v[222:223], s[34:35], 0, v[134:135]
	s_mov_b32 m0, s44
	s_nop 0
	global_load_lds_dwordx4 v[222:223], off
	s_waitcnt vmcnt(8)
	s_waitcnt lgkmcnt(0)
	s_barrier
	s_setprio 1
	s_waitcnt lgkmcnt(0)
	v_mfma_f32_16x16x32_bf16 v[126:129], v[144:147], v[182:185], v[126:129]
	v_mfma_f32_16x16x32_bf16 v[122:125], v[158:161], v[182:185], v[122:125]
	v_mfma_f32_16x16x32_bf16 v[110:113], v[144:147], v[190:193], v[110:113]
	v_mfma_f32_16x16x32_bf16 v[106:109], v[158:161], v[190:193], v[106:109]
	v_mfma_f32_16x16x32_bf16 v[94:97], v[144:147], v[198:201], v[94:97]
	v_mfma_f32_16x16x32_bf16 v[90:93], v[158:161], v[198:201], v[90:93]
	v_mfma_f32_16x16x32_bf16 v[78:81], v[144:147], v[206:209], v[78:81]
	v_mfma_f32_16x16x32_bf16 v[74:77], v[158:161], v[206:209], v[74:77]
	v_mfma_f32_16x16x32_bf16 v[126:129], v[148:151], v[186:189], v[126:129]
	v_mfma_f32_16x16x32_bf16 v[122:125], v[162:165], v[186:189], v[122:125]
	v_mfma_f32_16x16x32_bf16 v[110:113], v[148:151], v[194:197], v[110:113]
	v_mfma_f32_16x16x32_bf16 v[106:109], v[162:165], v[194:197], v[106:109]
	v_mfma_f32_16x16x32_bf16 v[94:97], v[148:151], v[202:205], v[94:97]
	v_mfma_f32_16x16x32_bf16 v[90:93], v[162:165], v[202:205], v[90:93]
	v_mfma_f32_16x16x32_bf16 v[78:81], v[148:151], v[210:213], v[78:81]
	v_mfma_f32_16x16x32_bf16 v[74:77], v[162:165], v[210:213], v[74:77]
	s_setprio 0
	s_setprio 1
	v_mfma_f32_16x16x32_bf16 v[118:121], v[166:169], v[182:185], v[118:121]
	v_mfma_f32_16x16x32_bf16 v[114:117], v[174:177], v[182:185], v[114:117]
	v_mfma_f32_16x16x32_bf16 v[102:105], v[166:169], v[190:193], v[102:105]
	v_mfma_f32_16x16x32_bf16 v[98:101], v[174:177], v[190:193], v[98:101]
	v_mfma_f32_16x16x32_bf16 v[86:89], v[166:169], v[198:201], v[86:89]
	v_mfma_f32_16x16x32_bf16 v[82:85], v[174:177], v[198:201], v[82:85]
	v_mfma_f32_16x16x32_bf16 v[70:73], v[166:169], v[206:209], v[70:73]
	v_mfma_f32_16x16x32_bf16 v[66:69], v[174:177], v[206:209], v[66:69]
	v_mfma_f32_16x16x32_bf16 v[118:121], v[170:173], v[186:189], v[118:121]
	v_mfma_f32_16x16x32_bf16 v[114:117], v[178:181], v[186:189], v[114:117]
	v_mfma_f32_16x16x32_bf16 v[102:105], v[170:173], v[194:197], v[102:105]
	v_mfma_f32_16x16x32_bf16 v[98:101], v[178:181], v[194:197], v[98:101]
	v_mfma_f32_16x16x32_bf16 v[86:89], v[170:173], v[202:205], v[86:89]
	v_mfma_f32_16x16x32_bf16 v[82:85], v[178:181], v[202:205], v[82:85]
	v_mfma_f32_16x16x32_bf16 v[70:73], v[170:173], v[210:213], v[70:73]
	v_mfma_f32_16x16x32_bf16 v[66:69], v[178:181], v[210:213], v[66:69]
	s_setprio 0
	s_barrier
; #define PG8_STAGE2(bufoff, gbase, v0, v1) do { \
;         __builtin_amdgcn_global_load_lds((const unsigned*)((const char*)(gbase) + (v0)), (LAS unsigned*)(lds + (bufoff) + ldsw), 16, 0, 0); \
;         __builtin_amdgcn_global_load_lds((const unsigned*)((const char*)(gbase) + (v1)), (LAS unsigned*)(lds + (bufoff) + ldsw + 8192), 16, 0, 0); } while (0)
; #define PG8_STAGE(bufoff, gbase, voff) PG8_STAGE2(bufoff, gbase, (voff)[0], (voff)[1])
; #define PG8_LDA(dst, b, h) do { _Pragma("unroll") for (int m = 0; m < 4; ++m) _Pragma("unroll") for (int k = 0; k < 2; ++k) dst[m][k] = *(const LAS bf16x8*)(lds + PG8_SA(b, h) + aoff + m * 2048 + k * 1024); } while (0)
; #define PG8_MMA(ai, bj, At, Bt) do { __builtin_amdgcn_s_setprio(1); _Pragma("unroll") for (int m = 0; m < 4; ++m) _Pragma("unroll") for (int n = 0; n < 2; ++n) _Pragma("unroll") for (int k = 0; k < 2; ++k) \
;         acc[ai][bj][m][n] = __builtin_amdgcn_mfma_f32_16x16x32_bf16(Bt[n][k], At[m][k], acc[ai][bj][m][n], 0, 0, 0); __builtin_amdgcn_s_setprio(0); } while (0)
; #define PG8_WAIT_V(n) asm volatile("s_waitcnt vmcnt(" #n ")" ::: "memory")
; #define PG8_WAIT_L(n) asm volatile("s_waitcnt lgkmcnt(" #n ")" ::: "memory")
; #define PG8_BAR __builtin_amdgcn_s_barrier()
; #define PG8_SCHED __builtin_amdgcn_sched_barrier(0)
; template <class Epi, class Sched, bool ALIGN_EPI, bool SP2, bool GATHER>
; DI void gemm_phase(LAS unsigned char* lds, const Gemm g, const Sched& S, const Epi& E) {
;     ...
;             PG8_LDA(At, 1, 1); PG8_STAGE(PG8_SB(1, 0), b3, voffB); PG8_STAGE(PG8_SB(1, 1), b3 + hstep, voffB); PG8_STAGE2(PG8_SA(1, 0), a3, x00, x01);
;             PG8_WAIT_V(8); PG8_WAIT_L(0); PG8_BAR; PG8_MMA(1, 0, At, B0); PG8_MMA(1, 1, At, B1); PG8_BAR; PG8_SCHED;
;         }
	s_add_i32 s34, s54, s41
	v_lshl_add_u64 v[214:215], v[214:215], 0, s[10:11]
	s_mov_b32 m0, s34
	ds_read_b128 v[182:185], v156 offset:49152
	ds_read_b128 v[186:189], v156 offset:50176
	ds_read_b128 v[190:193], v156 offset:51200
	ds_read_b128 v[194:197], v156 offset:52224
	ds_read_b128 v[198:201], v156 offset:53248
	ds_read_b128 v[202:205], v156 offset:54272
	ds_read_b128 v[206:209], v156 offset:55296
	ds_read_b128 v[210:213], v156 offset:56320
	global_load_lds_dwordx4 v[214:215], off
	s_add_i32 m0, s34, 0x2000
	s_add_u32 s30, s30, 0x20080
	v_lshl_add_u64 v[214:215], v[216:217], 0, s[10:11]
	s_addc_u32 s31, s31, 0
	s_add_i32 s34, s55, s41
	global_load_lds_dwordx4 v[214:215], off
	v_lshl_add_u64 v[214:215], s[30:31], 0, v[132:133]
	s_mov_b32 m0, s34
	s_nop 0
	global_load_lds_dwordx4 v[214:215], off
	v_lshl_add_u64 v[214:215], s[30:31], 0, v[136:137]
	s_add_i32 m0, s34, 0x2000
	s_nop 0
	global_load_lds_dwordx4 v[214:215], off
	v_lshl_add_u64 v[214:215], v[218:219], 0, s[10:11]
	s_mov_b32 m0, s46
	s_nop 0
	global_load_lds_dwordx4 v[214:215], off
	v_lshl_add_u64 v[214:215], v[220:221], 0, s[10:11]
	s_mov_b32 m0, s47
	s_nop 0
	global_load_lds_dwordx4 v[214:215], off
	s_waitcnt vmcnt(8)
	s_waitcnt lgkmcnt(0)
	s_barrier
	s_setprio 1
	s_waitcnt lgkmcnt(0)
	v_mfma_f32_16x16x32_bf16 v[62:65], v[144:147], v[182:185], v[62:65]
	v_mfma_f32_16x16x32_bf16 v[58:61], v[158:161], v[182:185], v[58:61]
	v_mfma_f32_16x16x32_bf16 v[46:49], v[144:147], v[190:193], v[46:49]
	v_mfma_f32_16x16x32_bf16 v[42:45], v[158:161], v[190:193], v[42:45]
	v_mfma_f32_16x16x32_bf16 v[14:17], v[144:147], v[198:201], v[14:17]
	v_mfma_f32_16x16x32_bf16 v[10:13], v[158:161], v[198:201], v[10:13]
	v_mfma_f32_16x16x32_bf16 v[6:9], v[144:147], v[206:209], v[6:9]
	v_mfma_f32_16x16x32_bf16 v[2:5], v[158:161], v[206:209], v[2:5]
	v_mfma_f32_16x16x32_bf16 v[62:65], v[148:151], v[186:189], v[62:65]
	v_mfma_f32_16x16x32_bf16 v[58:61], v[162:165], v[186:189], v[58:61]
	v_mfma_f32_16x16x32_bf16 v[46:49], v[148:151], v[194:197], v[46:49]
	v_mfma_f32_16x16x32_bf16 v[42:45], v[162:165], v[194:197], v[42:45]
	v_mfma_f32_16x16x32_bf16 v[14:17], v[148:151], v[202:205], v[14:17]
	v_mfma_f32_16x16x32_bf16 v[10:13], v[162:165], v[202:205], v[10:13]
	v_mfma_f32_16x16x32_bf16 v[6:9], v[148:151], v[210:213], v[6:9]
	v_mfma_f32_16x16x32_bf16 v[2:5], v[162:165], v[210:213], v[2:5]
	s_setprio 0
	s_setprio 1
	v_mfma_f32_16x16x32_bf16 v[54:57], v[166:169], v[182:185], v[54:57]
	v_mfma_f32_16x16x32_bf16 v[50:53], v[174:177], v[182:185], v[50:53]
	v_mfma_f32_16x16x32_bf16 v[30:33], v[166:169], v[190:193], v[30:33]
	v_mfma_f32_16x16x32_bf16 v[26:29], v[174:177], v[190:193], v[26:29]
	v_mfma_f32_16x16x32_bf16 v[34:37], v[166:169], v[198:201], v[34:37]
	v_mfma_f32_16x16x32_bf16 v[38:41], v[174:177], v[198:201], v[38:41]
	v_mfma_f32_16x16x32_bf16 v[18:21], v[166:169], v[206:209], v[18:21]
	v_mfma_f32_16x16x32_bf16 v[22:25], v[174:177], v[206:209], v[22:25]
	v_mfma_f32_16x16x32_bf16 v[54:57], v[170:173], v[186:189], v[54:57]
	v_mfma_f32_16x16x32_bf16 v[50:53], v[178:181], v[186:189], v[50:53]
	v_mfma_f32_16x16x32_bf16 v[30:33], v[170:173], v[194:197], v[30:33]
	v_mfma_f32_16x16x32_bf16 v[26:29], v[178:181], v[194:197], v[26:29]
	v_mfma_f32_16x16x32_bf16 v[34:37], v[170:173], v[202:205], v[34:37]
	v_mfma_f32_16x16x32_bf16 v[38:41], v[178:181], v[202:205], v[38:41]
	v_mfma_f32_16x16x32_bf16 v[18:21], v[170:173], v[210:213], v[18:21]
	v_mfma_f32_16x16x32_bf16 v[22:25], v[178:181], v[210:213], v[22:25]
	s_setprio 0
	s_barrier
	s_add_i32 s53, s53, 2
	s_add_u32 s28, s28, 0x100
	s_addc_u32 s29, s29, 0
	s_add_u32 s51, s51, 0x100
	s_addc_u32 s52, s52, 0
	s_cmp_gt_u32 s53, 5
	s_cbranch_scc1 .Lpeel_exit_p10
